# q_idx stored fragment-major (lane-contiguous indexer loads, coalesced stores) on top of scan rewrite + attention LUT masks
# speedup vs baseline: 1.0269x; 1.0004x over previous
; template <class Epi, class Sched, bool ALIGN_EPI = false, bool SP2 = false, bool FP8 = false, bool ABLK = false>
; __device__ __forceinline__ void gemm_phase(PG8_LAS unsigned char* lds, const Gemm g, const Sched& S, const Epi& E) {
;     ...
;     for (int i = 0; i < 2; ++i) { int R, C; stage_rc(tid * 16 + i * 8192, R, C); const int Rb = Epi::PERM ? ((R & ~31) + perm32(R & 31)) : R;
;         voffA[i] = ABLK ? (unsigned)(((((R >> 6) * 4 + (C >> 4)) * 8 + ((R >> 4) & 3)) * 64 + ((C >> 3) & 1) * 32 + (R & 15) * 2) * 8) : (unsigned)(R * K + C) * 2u; voffB[i] = (unsigned)(Rb * K + C) * 2u; }
;     const size_t kstep = (size_t)(BK * 2);
;     const size_t hstep = (size_t)HALF * K * 2;
;     const size_t kstepA = ABLK ? (size_t)32768 : kstep, hstepA = ABLK ? (size_t)2048 : hstep;
;     const size_t tstep = 2 * hstep;
;     const unsigned ldsw = (unsigned)wid * 1024u;
;     const int aoff = lds_byte(wr * 64 + fr, fq * 8), boff = lds_byte(wc * 32 + fr, fq * 8);
;     ...
;     Unit cur, nxt; int ui = 0;
;     if (!S.next(0, cur)) return;
;     f32x4 acc[2][2][4][2];
; #pragma unroll
;     for (int a = 0; a < 2; ++a)
; #pragma unroll
;         for (int b = 0; b < 2; ++b)
; #pragma unroll
;             for (int m = 0; m < 4; ++m)
; #pragma unroll
;                 for (int n = 0; n < 2; ++n) acc[a][b][m][n] = (f32x4){0.f, 0.f, 0.f, 0.f};
;     bf16x8 At[4][2], B0[2][2], B1[2][2];
;     const char* cA = (const char*)g.A + (size_t)cur.pm * tstep; const char* cB = (const char*)g.Bt + (size_t)cur.pn * tstep;
;     S.a_ready(cur);
;     if constexpr (SP2) {
;         PG8_STAGE(PG8_SB(0, 0), cB, voffB); PG8_STAGE(PG8_SB(0, 1), cB + hstep, voffB); PG8_STAGE(PG8_SA(0, 0), cA, voffA); PG8_STAGE(PG8_SA(0, 1), cA + hstepA, voffA);
;         if (wr == 1) PG8_BAR;
;         PG8_WAIT_V(2); PG8_BAR;
;         PG8_STAGE(PG8_SB(1, 0), cB + kstep, voffB); PG8_STAGE(PG8_SA(1, 0), cA + kstepA, voffA); PG8_STAGE(PG8_SB(1, 1), cB + hstep + kstep, voffB);
;         PG8_WAIT_V(0); PG8_BAR;
;     } else {
;         PG8_STAGE(PG8_SB(0, 0), cB, voffB); PG8_STAGE(PG8_SA(0, 0), cA, voffA); PG8_STAGE(PG8_SB(0, 1), cB + hstep, voffB); PG8_STAGE(PG8_SA(0, 1), cA + hstepA, voffA);
;         if (wr == 1) PG8_BAR;
;         PG8_WAIT_V(4); PG8_BAR;
;         PG8_STAGE(PG8_SB(1, 0), cB + kstep, voffB); PG8_STAGE(PG8_SA(1, 0), cA + kstepA, voffA); PG8_STAGE(PG8_SB(1, 1), cB + hstep + kstep, voffB);
.LBB0_587:
	s_add_u32 s50, s38, 0x1c200000
	s_addc_u32 s51, s39, 0
	s_add_u32 s52, s38, 0x300000
	s_addc_u32 s53, s39, 0
	s_add_u32 s22, s38, 0x15a00000
	s_addc_u32 s23, s39, 0
	s_add_u32 s56, s38, 0x400000
	v_writelane_b32 v252, s22, 28
	s_addc_u32 s57, s39, 0
	v_bfe_u32 v187, v18, 4, 2
	v_writelane_b32 v252, s23, 29
	s_add_u32 s22, s38, 0x15e00000
	s_addc_u32 s23, s39, 0
	s_add_u32 s60, s38, 0xda00000
	s_addc_u32 s61, s39, 0
	s_add_u32 s62, s38, 0x800000
	v_writelane_b32 v252, s22, 30
	s_addc_u32 s63, s39, 0
	s_add_u32 s19, s38, 0x10a00000
	v_writelane_b32 v252, s23, 31
	v_writelane_b32 v252, s19, 32
	s_addc_u32 s19, s39, 0
	v_writelane_b32 v252, s19, 33
	s_add_u32 s19, s38, 0xea00000
	v_writelane_b32 v252, s19, 34
	s_addc_u32 s19, s39, 0
	v_writelane_b32 v252, s19, 35
	s_add_u32 s19, s38, 0x12a00000
	v_writelane_b32 v252, s19, 36
	s_addc_u32 s19, s39, 0
	s_add_u32 s54, s38, 0xba00000
	v_and_b32_e32 v1, 15, v18
	v_lshlrev_b32_e32 v19, 4, v187
	v_lshlrev_b32_e32 v18, 2, v18
	s_addc_u32 s55, s39, 0
	s_and_b32 s40, s5, 3
	s_lshl_b32 s58, s4, 6
	v_lshl_or_b32 v19, v1, 6, v19
	s_lshl_b32 s4, s4, 13
	v_and_b32_e32 v18, 32, v18
	s_add_i32 m0, s8, 0x18000
	v_lshl_add_u64 v[10:11], v[10:11], 0, s[34:35]
	v_writelane_b32 v252, s19, 37
	v_bitop3_b32 v20, v19, s4, v18 bitop3:0xde
	s_lshl_b32 s59, s40, 5
	s_lshl_b32 s4, s40, 12
	s_waitcnt vmcnt(2)
	s_barrier
	global_load_lds_dwordx4 v[10:11], off
	v_lshl_add_u64 v[8:9], v[8:9], 0, s[34:35]
	s_add_i32 m0, s8, 0x1a000
	s_add_i32 s19, s8, 0x8000
	s_add_i32 s20, s8, 0xa000
	v_bitop3_b32 v191, v19, s4, v18 bitop3:0xde
	global_load_lds_dwordx4 v[8:9], off
	v_lshl_add_u64 v[4:5], v[4:5], 0, s[34:35]
	s_mov_b32 m0, s19
	s_add_u32 s4, s44, 0x40080
	global_load_lds_dwordx4 v[4:5], off
	v_lshl_add_u64 v[4:5], v[6:7], 0, s[34:35]
	s_mov_b32 m0, s20
	s_addc_u32 s5, s45, 0
	global_load_lds_dwordx4 v[4:5], off
	s_add_i32 m0, s8, 0x1c000
	v_lshl_add_u64 v[4:5], s[4:5], 0, v[2:3]
	global_load_lds_dwordx4 v[4:5], off
	v_lshl_add_u64 v[4:5], s[4:5], 0, v[172:173]
	s_add_i32 m0, s8, 0x1e000
	s_cmpk_lt_u32 s21, 0x100
	global_load_lds_dwordx4 v[4:5], off
	s_cselect_b64 s[64:65], -1, 0
	s_add_i32 s21, s58, 0xffff0c00
	s_cmp_eq_u32 s40, 0
	v_lshlrev_b32_e32 v4, 14, v16
	s_cselect_b64 s[66:67], -1, 0
	s_cmp_eq_u32 s40, 1
	v_and_b32_e32 v4, 0xffff8000, v4
	s_cselect_b64 s[68:69], -1, 0
	s_lshl_b32 s4, s40, 6
	v_lshl_add_u32 v4, v15, 11, v4
	v_and_b32_e32 v5, 1, v16
	s_or_b32 s23, s4, 0xfffff900
	s_or_b32 s81, s4, 0xfffffb00
	s_lshl_b32 s4, s40, 12
	v_lshl_or_b32 v4, v5, 6, v4
	s_add_u32 s4, s38, s4
	v_lshl_add_u32 v178, v17, 1, v4
	v_lshlrev_b32_e32 v4, 14, v12
	s_addc_u32 s5, s39, 0
	v_and_b32_e32 v4, 0xffff8000, v4
	s_waitcnt vmcnt(0)
	s_add_u32 s70, s4, 0x14a00000
	v_lshl_add_u32 v4, v13, 11, v4
	v_and_b32_e32 v5, 1, v12
	s_addc_u32 s71, s5, 0
	v_lshl_or_b32 v4, v5, 6, v4
	v_readlane_b32 s4, v254, 42
	s_mov_b32 s47, s93
	s_mov_b32 s22, 0
	v_mov_b32_e32 v179, v3
	v_lshl_add_u32 v180, v14, 1, v4
	v_mov_b32_e32 v181, v3
	v_add_u32_e32 v195, 0, v20
	s_mov_b32 s73, s4
	s_barrier
	v_readlane_b32 s5, v254, 43
	s_branch .LBB0_590

; __device__ __forceinline__ float rstd_fin4(const f32x4 a) { float s = (a[0] + a[1]) + (a[2] + a[3]); s += __shfl_xor(s, 16); s += __shfl_xor(s, 32); return __builtin_amdgcn_rsqf(s * (1.f / 1024.f) + 1e-6f); }
;     __device__ __forceinline__ void operator()(const f32x4 (&acc)[2][2][4][2], const Unit& u, int wr, int wc, int fr, int fq) const {
;     ...
;         float rsv[8];
;         { f32x4 pa[8];
; #pragma unroll
;           for (int q = 0; q < 8; ++q) pa[q] = rstd_ld4(ss, row0 + (q >> 2) * HALF + (q & 3) * 16, fq);
; #pragma unroll
;           for (int q = 0; q < 8; ++q) rsv[q] = rstd_fin4(pa[q]); }
;         asm volatile("" ::: "memory");
.LBB0_654:
	s_lshl_b32 s4, s73, 8
	v_mov_b32_e32 v211, v1
	v_mov_b32_e32 v132, v187
	s_add_i32 s4, s21, s4
	v_and_b32_e32 v166, 64, v246
	v_add_u32_e32 v220, s4, v211
	v_lshlrev_b32_e32 v134, 2, v132
	v_add_u32_e32 v216, 16, v220
	v_ashrrev_i32_e32 v135, 31, v134
	v_ashrrev_i32_e32 v221, 31, v220
	v_ashrrev_i32_e32 v217, 31, v216
	v_add_u32_e32 v212, 32, v220
	v_add_u32_e32 v208, 48, v220
	v_lshl_add_u64 v[162:163], v[134:135], 2, s[50:51]
	v_lshlrev_b64 v[134:135], 6, v[220:221]
	v_lshlrev_b64 v[136:137], 6, v[216:217]
	v_ashrrev_i32_e32 v213, 31, v212
	v_ashrrev_i32_e32 v209, 31, v208
	v_lshl_add_u64 v[134:135], v[162:163], 0, v[134:135]
	v_lshl_add_u64 v[138:139], v[162:163], 0, v[136:137]
	v_lshlrev_b64 v[142:143], 6, v[212:213]
	v_lshlrev_b64 v[144:145], 6, v[208:209]
	global_load_dwordx4 v[134:137], v[134:135], off
	s_nop 0
	global_load_dwordx4 v[138:141], v[138:139], off
	v_lshl_add_u64 v[142:143], v[162:163], 0, v[142:143]
	v_lshl_add_u64 v[146:147], v[162:163], 0, v[144:145]
	v_add_u32_e32 v192, 0x80, v220
	global_load_dwordx4 v[142:145], v[142:143], off
	s_nop 0
	global_load_dwordx4 v[146:149], v[146:147], off
	v_ashrrev_i32_e32 v193, 31, v192
	v_lshlrev_b64 v[150:151], 6, v[192:193]
	v_lshl_add_u64 v[150:151], v[162:163], 0, v[150:151]
	global_load_dwordx4 v[150:153], v[150:151], off
	v_add_u32_e32 v188, 0x90, v220
	v_ashrrev_i32_e32 v189, 31, v188
	v_lshlrev_b64 v[154:155], 6, v[188:189]
	v_lshl_add_u64 v[154:155], v[162:163], 0, v[154:155]
	global_load_dwordx4 v[154:157], v[154:155], off
	v_add_u32_e32 v184, 0xa0, v220
	v_add_u32_e32 v182, 0xb0, v220
	v_ashrrev_i32_e32 v185, 31, v184
	v_ashrrev_i32_e32 v183, 31, v182
	v_lshlrev_b64 v[158:159], 6, v[184:185]
	v_lshlrev_b64 v[164:165], 6, v[182:183]
	v_lshl_add_u64 v[158:159], v[162:163], 0, v[158:159]
	v_lshl_add_u64 v[162:163], v[162:163], 0, v[164:165]
	global_load_dwordx4 v[158:161], v[158:159], off
	v_xor_b32_e32 v133, 16, v246
	global_load_dwordx4 v[162:165], v[162:163], off
	v_add_u32_e32 v166, 64, v166
	v_cmp_lt_i32_e32 vcc, v133, v166
	v_xor_b32_e32 v167, 32, v246
	v_cmp_lt_i32_e64 s[42:43], v167, v166
	v_cndmask_b32_e32 v133, v246, v133, vcc
	v_lshlrev_b32_e32 v133, 2, v133
	v_cndmask_b32_e64 v166, v246, v167, s[42:43]
	v_lshlrev_b32_e32 v166, 2, v166
	s_sub_i32 s75, s72, s6
	s_cmp_gt_i32 s75, 4
	s_cselect_b64 s[4:5], -1, 0
	s_add_i32 s42, s75, -9
	s_cmp_gt_u32 s42, 1
	s_cselect_b64 s[42:43], -1, 0
	s_and_b64 s[42:43], s[4:5], s[42:43]
	v_lshlrev_b32_e32 v224, 3, v132
	s_mov_b64 s[4:5], -1
	s_and_b64 vcc, exec, s[42:43]
	s_waitcnt vmcnt(0)
	v_add_f32_e32 v134, v134, v135
	v_add_f32_e32 v135, v136, v137
	v_add_f32_e32 v134, v134, v135
	v_add_f32_e32 v135, v138, v139
	v_add_f32_e32 v136, v140, v141
	v_add_f32_e32 v137, v142, v143
	v_add_f32_e32 v138, v144, v145
	v_add_f32_e32 v139, v146, v147
	v_add_f32_e32 v140, v148, v149
	ds_bpermute_b32 v145, v133, v134
	v_add_f32_e32 v135, v135, v136
	v_add_f32_e32 v136, v137, v138
	v_add_f32_e32 v137, v139, v140
	ds_bpermute_b32 v139, v133, v135
	ds_bpermute_b32 v140, v133, v136
	v_add_f32_e32 v141, v150, v151
	v_add_f32_e32 v142, v152, v153
	v_add_f32_e32 v138, v141, v142
	ds_bpermute_b32 v141, v133, v137
	s_waitcnt lgkmcnt(3)
	v_add_f32_e32 v134, v134, v145
	ds_bpermute_b32 v142, v133, v138
	ds_bpermute_b32 v145, v166, v134
	s_waitcnt lgkmcnt(4)
	v_add_f32_e32 v135, v135, v139
	s_waitcnt lgkmcnt(3)
	v_add_f32_e32 v136, v136, v140
	ds_bpermute_b32 v139, v166, v135
	ds_bpermute_b32 v140, v166, v136
	s_waitcnt lgkmcnt(4)
	v_add_f32_e32 v137, v137, v141
	ds_bpermute_b32 v141, v166, v137
	s_waitcnt lgkmcnt(4)
	v_add_f32_e32 v138, v138, v142
	s_waitcnt lgkmcnt(3)
	v_add_f32_e32 v134, v134, v145
	ds_bpermute_b32 v142, v166, v138
	v_fmamk_f32 v134, v134, 0x3a800000, v227
	s_waitcnt lgkmcnt(3)
	v_add_f32_e32 v135, v135, v139
	v_add_f32_e32 v143, v154, v155
	v_add_f32_e32 v144, v156, v157
	s_waitcnt lgkmcnt(2)
	v_add_f32_e32 v136, v136, v140
	v_rsq_f32_e32 v226, v134
	v_fmamk_f32 v134, v135, 0x3a800000, v227
	v_fmamk_f32 v135, v136, 0x3a800000, v227
	v_rsq_f32_e32 v222, v134
	v_add_f32_e32 v134, v143, v144
	s_waitcnt lgkmcnt(1)
	v_add_f32_e32 v137, v137, v141
	v_rsq_f32_e32 v218, v135
	ds_bpermute_b32 v135, v133, v134
	v_fmamk_f32 v136, v137, 0x3a800000, v227
	v_rsq_f32_e32 v214, v136
	s_waitcnt lgkmcnt(1)
	v_add_f32_e32 v136, v138, v142
	v_fmamk_f32 v136, v136, 0x3a800000, v227
	v_rsq_f32_e32 v210, v136
	v_add_f32_e32 v136, v158, v159
	v_add_f32_e32 v137, v160, v161
	v_add_f32_e32 v138, v162, v163
	v_add_f32_e32 v139, v164, v165
	s_waitcnt lgkmcnt(0)
	v_add_f32_e32 v134, v134, v135
	v_add_f32_e32 v136, v136, v137
	v_add_f32_e32 v138, v138, v139
	ds_bpermute_b32 v135, v166, v134
	ds_bpermute_b32 v137, v133, v136
	ds_bpermute_b32 v133, v133, v138
	s_waitcnt lgkmcnt(2)
	v_add_f32_e32 v134, v134, v135
	s_waitcnt lgkmcnt(1)
	v_add_f32_e32 v135, v136, v137
	s_waitcnt lgkmcnt(0)
	v_add_f32_e32 v133, v138, v133
	ds_bpermute_b32 v136, v166, v135
	ds_bpermute_b32 v137, v166, v133
	v_fmamk_f32 v134, v134, 0x3a800000, v227
	v_rsq_f32_e32 v194, v134
	s_waitcnt lgkmcnt(1)
	v_add_f32_e32 v134, v135, v136
	s_waitcnt lgkmcnt(0)
	v_add_f32_e32 v133, v133, v137
	v_fmamk_f32 v134, v134, 0x3a800000, v227
	v_fmamk_f32 v133, v133, 0x3a800000, v227
	v_rsq_f32_e32 v190, v134
	v_rsq_f32_e32 v186, v133
	s_cbranch_vccz .LBB0_776
; __device__ __forceinline__ u32x4 pack8(const f32x4 a, const f32x4 b) { u32x4 w; w.x = cvt_pk_bf16(a[0], a[1]); w.y = cvt_pk_bf16(a[2], a[3]); w.z = cvt_pk_bf16(b[0], b[1]); w.w = cvt_pk_bf16(b[2], b[3]); return w; }
;     __device__ __forceinline__ void operator()(const f32x4 (&acc)[2][2][4][2], const Unit& u, int wr, int wc, int fr, int fq) const {
;     ...
;             f32x4 cc[4], cn[4];
;             { const size_t o = (size_t)row0 * 32 + fq * 8; cc[0] = *(const f32x4*)(cs + o); cc[1] = *(const f32x4*)(cs + o + 4); cc[2] = *(const f32x4*)(sn + o); cc[3] = *(const f32x4*)(sn + o + 4); }
; #pragma unroll
;             for (int q = 0; q < 8; ++q) { const int ai = q >> 2, m = q & 3; const int row = row0 + ai * HALF + m * 16; const float rs = rsv[q];
;                 if (q + 1 < 8) { const size_t o = (size_t)(row0 + ((q + 1) >> 2) * HALF + ((q + 1) & 3) * 16) * 32 + fq * 8; cn[0] = *(const f32x4*)(cs + o); cn[1] = *(const f32x4*)(cs + o + 4); cn[2] = *(const f32x4*)(sn + o); cn[3] = *(const f32x4*)(sn + o + 4); }
;                 const f32x4 a0 = acc[ai][0][m][0] * rs, a1 = acc[ai][0][m][1] * rs, b0 = acc[ai][1][m][0] * rs, b1 = acc[ai][1][m][1] * rs;
;                 const f32x4 c0 = cc[0], c1 = cc[1], s0 = cc[2], s1 = cc[3];
;                 f32x4 p0 = a0 * c0 - b0 * s0, p1 = a1 * c1 - b1 * s1, r0 = b0 * c0 + a0 * s0, r1 = b1 * c1 + a1 * s1;
;                 if (t < 7) { bf16_t* d = Q + (size_t)row * 512 + ((t - 5) * 4 + wc) * 64 + fq * 8; *(u32x4*)d = pack8(p0 * qscale, p1 * qscale); *(u32x4*)(d + 32) = pack8(r0 * qscale, r1 * qscale); }
	v_lshlrev_b64 v[134:135], 5, v[220:221]
	v_ashrrev_i32_e32 v225, 31, v224
	v_lshl_add_u64 v[134:135], v[134:135], 0, v[224:225]
	v_lshlrev_b64 v[134:135], 2, v[134:135]
	v_lshl_add_u64 v[136:137], s[56:57], 0, v[134:135]
	v_lshl_add_u64 v[134:135], s[62:63], 0, v[134:135]
	global_load_dwordx4 v[234:237], v[136:137], off offset:16
	global_load_dwordx4 v[154:157], v[136:137], off
	global_load_dwordx4 v[238:241], v[134:135], off offset:16
	global_load_dwordx4 v[158:161], v[134:135], off
	v_ashrrev_i32_e32 v134, 1, v132
	v_ashrrev_i32_e32 v135, 31, v134
	v_lshlrev_b64 v[232:233], 6, v[134:135]
	v_lshlrev_b32_e32 v133, 5, v132
	v_and_or_b32 v232, v133, 32, v232
	v_cmp_eq_u32_e32 vcc, 0, v132
	v_lshlrev_b64 v[132:133], 5, v[216:217]
	v_lshl_add_u64 v[132:133], v[132:133], 0, v[224:225]
	v_lshlrev_b64 v[140:141], 2, v[132:133]
	v_lshl_add_u64 v[136:137], s[56:57], 0, v[140:141]
	v_lshl_add_u64 v[144:145], s[62:63], 0, v[140:141]
	global_load_dwordx4 v[132:135], v[136:137], off offset:16
	s_nop 0
	global_load_dwordx4 v[136:139], v[136:137], off
	s_nop 0
	global_load_dwordx4 v[140:143], v[144:145], off offset:16
	s_nop 0
	global_load_dwordx4 v[144:147], v[144:145], off
	s_cmp_gt_u32 s75, 6
	s_cselect_b64 s[42:43], -1, 0
	s_cmp_gt_u32 s75, 8
	s_cselect_b64 s[94:95], -1, 0
	s_cmp_lg_u32 s75, 11
	s_cselect_b64 s[90:91], -1, 0
	s_lshl_b32 s44, s75, 8
	s_add_i32 s92, s23, s44
	s_and_b64 s[72:73], s[68:69], vcc
	s_lshl_b64 s[4:5], s[92:93], 1
	v_readlane_b32 s45, v252, 32
	s_add_u32 s4, s45, s4
	v_readlane_b32 s45, v252, 33
	v_lshlrev_b64 v[152:153], 1, v[224:225]
	s_addc_u32 s5, s45, s5
	s_add_i32 s92, s81, s44
	v_pk_mul_f32 v[170:171], v[130:131], v[226:227] op_sel_hi:[1,0]
	v_pk_mul_f32 v[242:243], v[128:129], v[226:227] op_sel_hi:[1,0]
	v_pk_mul_f32 v[150:151], v[122:123], v[226:227] op_sel_hi:[1,0]
	v_pk_mul_f32 v[148:149], v[120:121], v[226:227] op_sel_hi:[1,0]
	v_lshl_add_u64 v[228:229], s[4:5], 0, v[152:153]
	s_lshl_b64 s[4:5], s[92:93], 1
	v_readlane_b32 s44, v252, 34
	v_pk_mul_f32 v[248:249], v[126:127], v[226:227] op_sel_hi:[1,0]
	v_pk_mul_f32 v[250:251], v[124:125], v[226:227] op_sel_hi:[1,0]
	v_pk_mul_f32 v[204:205], v[118:119], v[226:227] op_sel_hi:[1,0]
	v_pk_mul_f32 v[206:207], v[116:117], v[226:227] op_sel_hi:[1,0]
	s_add_u32 s44, s44, s4
	v_readlane_b32 s4, v252, 35
	v_mov_b64_e32 v[202:203], 0x200
	v_mov_b64_e32 v[200:201], 0xaff
	v_mov_b64_e32 v[198:199], 0xb00
	v_mov_b64_e32 v[196:197], 0x900
	v_lshlrev_b32_e32 v230, 6, v224
	v_mov_b32_e32 v231, 0
	v_lshl_add_u64 v[230:231], v[230:231], 0, s[70:71]
	s_addc_u32 s45, s4, s5
	s_mov_b64 s[96:97], -1
	s_and_b64 vcc, exec, s[42:43]
	s_waitcnt vmcnt(4)
	v_pk_mul_f32 v[162:163], v[150:151], v[160:161]
	v_pk_mul_f32 v[166:167], v[148:149], v[158:159]
	v_pk_mul_f32 v[160:161], v[170:171], v[160:161]
	v_pk_mul_f32 v[158:159], v[242:243], v[158:159]
	v_pk_fma_f32 v[164:165], v[170:171], v[156:157], v[162:163] neg_lo:[0,0,1] neg_hi:[0,0,1]
	v_pk_fma_f32 v[168:169], v[242:243], v[154:155], v[166:167] neg_lo:[0,0,1] neg_hi:[0,0,1]
	v_pk_mul_f32 v[162:163], v[204:205], v[240:241]
	v_pk_mul_f32 v[166:167], v[206:207], v[238:239]
	v_pk_fma_f32 v[156:157], v[150:151], v[156:157], v[160:161]
	v_pk_fma_f32 v[160:161], v[148:149], v[154:155], v[158:159]
	v_pk_mul_f32 v[154:155], v[248:249], v[240:241]
	v_pk_mul_f32 v[158:159], v[250:251], v[238:239]
	v_pk_fma_f32 v[162:163], v[248:249], v[236:237], v[162:163] neg_lo:[0,0,1] neg_hi:[0,0,1]
	v_pk_fma_f32 v[166:167], v[250:251], v[234:235], v[166:167] neg_lo:[0,0,1] neg_hi:[0,0,1]
	v_pk_fma_f32 v[154:155], v[204:205], v[236:237], v[154:155]
	v_pk_fma_f32 v[158:159], v[206:207], v[234:235], v[158:159]
	s_cbranch_vccz .LBB0_668
	s_mov_b64 s[4:5], -1
	s_and_b64 vcc, exec, s[94:95]
	s_cbranch_vccz .LBB0_665
	s_and_b64 vcc, exec, s[90:91]
	s_cbranch_vccz .LBB0_662
	s_andn2_b64 vcc, exec, s[66:67]
	s_cbranch_vccz .LBB0_877
	s_and_saveexec_b64 s[4:5], s[72:73]
	s_cbranch_execz .LBB0_661

; __device__ __forceinline__ u32x4 pack8(const f32x4 a, const f32x4 b) { u32x4 w; w.x = cvt_pk_bf16(a[0], a[1]); w.y = cvt_pk_bf16(a[2], a[3]); w.z = cvt_pk_bf16(b[0], b[1]); w.w = cvt_pk_bf16(b[2], b[3]); return w; }
;     __device__ __forceinline__ void operator()(const f32x4 (&acc)[2][2][4][2], const Unit& u, int wr, int wc, int fr, int fq) const {
;     ...
;             for (int q = 0; q < 8; ++q) { const int ai = q >> 2, m = q & 3; const int row = row0 + ai * HALF + m * 16; const float rs = rsv[q];
;                 if (q + 1 < 8) { const size_t o = (size_t)(row0 + ((q + 1) >> 2) * HALF + ((q + 1) & 3) * 16) * 32 + fq * 8; cn[0] = *(const f32x4*)(cs + o); cn[1] = *(const f32x4*)(cs + o + 4); cn[2] = *(const f32x4*)(sn + o); cn[3] = *(const f32x4*)(sn + o + 4); }
;                 const f32x4 a0 = acc[ai][0][m][0] * rs, a1 = acc[ai][0][m][1] * rs, b0 = acc[ai][1][m][0] * rs, b1 = acc[ai][1][m][1] * rs;
;                 const f32x4 c0 = cc[0], c1 = cc[1], s0 = cc[2], s1 = cc[3];
;                 f32x4 p0 = a0 * c0 - b0 * s0, p1 = a1 * c1 - b1 * s1, r0 = b0 * c0 + a0 * s0, r1 = b1 * c1 + a1 * s1;
;                 if (t < 7) { bf16_t* d = Q + (size_t)row * 512 + ((t - 5) * 4 + wc) * 64 + fq * 8; *(u32x4*)d = pack8(p0 * qscale, p1 * qscale); *(u32x4*)(d + 32) = pack8(r0 * qscale, r1 * qscale); }
;                 else if (t < 9) { bf16_t* d = K + (size_t)row * 512 + ((t - 7) * 4 + wc) * 64 + fq * 8; *(u32x4*)d = pack8(p0, p1); *(u32x4*)(d + 32) = pack8(r0, r1); }
;                 else if (t == 11) { bf16_t* d = QI + (size_t)row * 256 + wc * 64 + fq * 8; *(u32x4*)d = pack8(p0, p1); *(u32x4*)(d + 32) = pack8(r0, r1); }
.LBB0_662:
	s_and_b64 vcc, exec, s[4:5]
	s_cbranch_vccz .LBB0_664
	v_and_b32_e32 v148, -32, v220
	v_lshlrev_b32_e32 v148, 9, v148
	v_and_b32_e32 v149, 31, v220
	v_lshl_add_u32 v148, v149, 4, v148
	v_mov_b32_e32 v149, 0
	v_lshl_add_u64 v[170:171], v[230:231], 0, v[148:149]
	v_cvt_pk_bf16_f32 v148, v168, v169
	v_cvt_pk_bf16_f32 v149, v164, v165
	v_cvt_pk_bf16_f32 v150, v166, v167
	v_cvt_pk_bf16_f32 v151, v162, v163
	global_store_dwordx4 v[170:171], v[148:151], off
	s_nop 1
	v_cvt_pk_bf16_f32 v148, v160, v161
	v_cvt_pk_bf16_f32 v149, v156, v157
	v_cvt_pk_bf16_f32 v150, v158, v159
	v_cvt_pk_bf16_f32 v151, v154, v155
	global_store_dwordx4 v[170:171], v[148:151], off offset:2048

; __device__ __forceinline__ u32x4 pack8(const f32x4 a, const f32x4 b) { u32x4 w; w.x = cvt_pk_bf16(a[0], a[1]); w.y = cvt_pk_bf16(a[2], a[3]); w.z = cvt_pk_bf16(b[0], b[1]); w.w = cvt_pk_bf16(b[2], b[3]); return w; }
;     __device__ __forceinline__ void operator()(const f32x4 (&acc)[2][2][4][2], const Unit& u, int wr, int wc, int fr, int fq) const {
;     ...
;             for (int q = 0; q < 8; ++q) { const int ai = q >> 2, m = q & 3; const int row = row0 + ai * HALF + m * 16; const float rs = rsv[q];
;                 if (q + 1 < 8) { const size_t o = (size_t)(row0 + ((q + 1) >> 2) * HALF + ((q + 1) & 3) * 16) * 32 + fq * 8; cn[0] = *(const f32x4*)(cs + o); cn[1] = *(const f32x4*)(cs + o + 4); cn[2] = *(const f32x4*)(sn + o); cn[3] = *(const f32x4*)(sn + o + 4); }
;                 const f32x4 a0 = acc[ai][0][m][0] * rs, a1 = acc[ai][0][m][1] * rs, b0 = acc[ai][1][m][0] * rs, b1 = acc[ai][1][m][1] * rs;
;                 const f32x4 c0 = cc[0], c1 = cc[1], s0 = cc[2], s1 = cc[3];
;                 f32x4 p0 = a0 * c0 - b0 * s0, p1 = a1 * c1 - b1 * s1, r0 = b0 * c0 + a0 * s0, r1 = b1 * c1 + a1 * s1;
;                 if (t < 7) { bf16_t* d = Q + (size_t)row * 512 + ((t - 5) * 4 + wc) * 64 + fq * 8; *(u32x4*)d = pack8(p0 * qscale, p1 * qscale); *(u32x4*)(d + 32) = pack8(r0 * qscale, r1 * qscale); }
;                 else if (t < 9) { bf16_t* d = K + (size_t)row * 512 + ((t - 7) * 4 + wc) * 64 + fq * 8; *(u32x4*)d = pack8(p0, p1); *(u32x4*)(d + 32) = pack8(r0, r1); }
;                 else if (t == 11) { bf16_t* d = QI + (size_t)row * 256 + wc * 64 + fq * 8; *(u32x4*)d = pack8(p0, p1); *(u32x4*)(d + 32) = pack8(r0, r1); }
.LBB0_677:
	s_and_b64 vcc, exec, s[4:5]
	s_cbranch_vccz .LBB0_679
	v_and_b32_e32 v140, -32, v216
	v_lshlrev_b32_e32 v140, 9, v140
	v_and_b32_e32 v141, 31, v216
	v_lshl_add_u32 v140, v141, 4, v140
	v_mov_b32_e32 v141, 0
	v_lshl_add_u64 v[144:145], v[230:231], 0, v[140:141]
	v_cvt_pk_bf16_f32 v140, v170, v171
	v_cvt_pk_bf16_f32 v141, v168, v169
	v_cvt_pk_bf16_f32 v142, v238, v239
	v_cvt_pk_bf16_f32 v143, v236, v237
	global_store_dwordx4 v[144:145], v[140:143], off
	s_nop 1
	v_cvt_pk_bf16_f32 v140, v136, v137
	v_cvt_pk_bf16_f32 v141, v138, v139
	v_cvt_pk_bf16_f32 v142, v132, v133
	v_cvt_pk_bf16_f32 v143, v134, v135
	global_store_dwordx4 v[144:145], v[140:143], off offset:2048

; __device__ __forceinline__ u32x4 pack8(const f32x4 a, const f32x4 b) { u32x4 w; w.x = cvt_pk_bf16(a[0], a[1]); w.y = cvt_pk_bf16(a[2], a[3]); w.z = cvt_pk_bf16(b[0], b[1]); w.w = cvt_pk_bf16(b[2], b[3]); return w; }
;     __device__ __forceinline__ void operator()(const f32x4 (&acc)[2][2][4][2], const Unit& u, int wr, int wc, int fr, int fq) const {
;     ...
;             for (int q = 0; q < 8; ++q) { const int ai = q >> 2, m = q & 3; const int row = row0 + ai * HALF + m * 16; const float rs = rsv[q];
;                 if (q + 1 < 8) { const size_t o = (size_t)(row0 + ((q + 1) >> 2) * HALF + ((q + 1) & 3) * 16) * 32 + fq * 8; cn[0] = *(const f32x4*)(cs + o); cn[1] = *(const f32x4*)(cs + o + 4); cn[2] = *(const f32x4*)(sn + o); cn[3] = *(const f32x4*)(sn + o + 4); }
;                 const f32x4 a0 = acc[ai][0][m][0] * rs, a1 = acc[ai][0][m][1] * rs, b0 = acc[ai][1][m][0] * rs, b1 = acc[ai][1][m][1] * rs;
;                 const f32x4 c0 = cc[0], c1 = cc[1], s0 = cc[2], s1 = cc[3];
;                 f32x4 p0 = a0 * c0 - b0 * s0, p1 = a1 * c1 - b1 * s1, r0 = b0 * c0 + a0 * s0, r1 = b1 * c1 + a1 * s1;
;                 if (t < 7) { bf16_t* d = Q + (size_t)row * 512 + ((t - 5) * 4 + wc) * 64 + fq * 8; *(u32x4*)d = pack8(p0 * qscale, p1 * qscale); *(u32x4*)(d + 32) = pack8(r0 * qscale, r1 * qscale); }
;                 else if (t < 9) { bf16_t* d = K + (size_t)row * 512 + ((t - 7) * 4 + wc) * 64 + fq * 8; *(u32x4*)d = pack8(p0, p1); *(u32x4*)(d + 32) = pack8(r0, r1); }
;                 else if (t == 11) { bf16_t* d = QI + (size_t)row * 256 + wc * 64 + fq * 8; *(u32x4*)d = pack8(p0, p1); *(u32x4*)(d + 32) = pack8(r0, r1); }
.LBB0_692:
	s_and_b64 vcc, exec, s[4:5]
	s_cbranch_vccz .LBB0_694
	v_and_b32_e32 v136, -32, v212
	v_lshlrev_b32_e32 v136, 9, v136
	v_and_b32_e32 v137, 31, v212
	v_lshl_add_u32 v136, v137, 4, v136
	v_mov_b32_e32 v137, 0
	v_lshl_add_u64 v[152:153], v[230:231], 0, v[136:137]
	v_cvt_pk_bf16_f32 v136, v238, v239
	v_cvt_pk_bf16_f32 v137, v236, v237
	v_cvt_pk_bf16_f32 v138, v242, v243
	v_cvt_pk_bf16_f32 v139, v240, v241
	global_store_dwordx4 v[152:153], v[136:139], off
	s_nop 1
	v_cvt_pk_bf16_f32 v136, v146, v147
	v_cvt_pk_bf16_f32 v137, v144, v145
	v_cvt_pk_bf16_f32 v138, v148, v149
	v_cvt_pk_bf16_f32 v139, v150, v151
	global_store_dwordx4 v[152:153], v[136:139], off offset:2048

; __device__ __forceinline__ u32x4 pack8(const f32x4 a, const f32x4 b) { u32x4 w; w.x = cvt_pk_bf16(a[0], a[1]); w.y = cvt_pk_bf16(a[2], a[3]); w.z = cvt_pk_bf16(b[0], b[1]); w.w = cvt_pk_bf16(b[2], b[3]); return w; }
;     __device__ __forceinline__ void operator()(const f32x4 (&acc)[2][2][4][2], const Unit& u, int wr, int wc, int fr, int fq) const {
;     ...
;             for (int q = 0; q < 8; ++q) { const int ai = q >> 2, m = q & 3; const int row = row0 + ai * HALF + m * 16; const float rs = rsv[q];
;                 if (q + 1 < 8) { const size_t o = (size_t)(row0 + ((q + 1) >> 2) * HALF + ((q + 1) & 3) * 16) * 32 + fq * 8; cn[0] = *(const f32x4*)(cs + o); cn[1] = *(const f32x4*)(cs + o + 4); cn[2] = *(const f32x4*)(sn + o); cn[3] = *(const f32x4*)(sn + o + 4); }
;                 const f32x4 a0 = acc[ai][0][m][0] * rs, a1 = acc[ai][0][m][1] * rs, b0 = acc[ai][1][m][0] * rs, b1 = acc[ai][1][m][1] * rs;
;                 const f32x4 c0 = cc[0], c1 = cc[1], s0 = cc[2], s1 = cc[3];
;                 f32x4 p0 = a0 * c0 - b0 * s0, p1 = a1 * c1 - b1 * s1, r0 = b0 * c0 + a0 * s0, r1 = b1 * c1 + a1 * s1;
;                 if (t < 7) { bf16_t* d = Q + (size_t)row * 512 + ((t - 5) * 4 + wc) * 64 + fq * 8; *(u32x4*)d = pack8(p0 * qscale, p1 * qscale); *(u32x4*)(d + 32) = pack8(r0 * qscale, r1 * qscale); }
;                 else if (t < 9) { bf16_t* d = K + (size_t)row * 512 + ((t - 7) * 4 + wc) * 64 + fq * 8; *(u32x4*)d = pack8(p0, p1); *(u32x4*)(d + 32) = pack8(r0, r1); }
;                 else if (t == 11) { bf16_t* d = QI + (size_t)row * 256 + wc * 64 + fq * 8; *(u32x4*)d = pack8(p0, p1); *(u32x4*)(d + 32) = pack8(r0, r1); }
.LBB0_707:
	s_and_b64 vcc, exec, s[4:5]
	s_cbranch_vccz .LBB0_709
	v_and_b32_e32 v140, -32, v208
	v_lshlrev_b32_e32 v140, 9, v140
	v_and_b32_e32 v141, 31, v208
	v_lshl_add_u32 v140, v141, 4, v140
	v_mov_b32_e32 v141, 0
	v_lshl_add_u64 v[152:153], v[230:231], 0, v[140:141]
	v_cvt_pk_bf16_f32 v140, v166, v167
	v_cvt_pk_bf16_f32 v141, v164, v165
	v_cvt_pk_bf16_f32 v142, v238, v239
	v_cvt_pk_bf16_f32 v143, v236, v237
	global_store_dwordx4 v[152:153], v[140:143], off
	s_nop 1
	v_cvt_pk_bf16_f32 v140, v160, v161
	v_cvt_pk_bf16_f32 v141, v162, v163
	v_cvt_pk_bf16_f32 v142, v132, v133
	v_cvt_pk_bf16_f32 v143, v134, v135
	global_store_dwordx4 v[152:153], v[140:143], off offset:2048

; __device__ __forceinline__ u32x4 pack8(const f32x4 a, const f32x4 b) { u32x4 w; w.x = cvt_pk_bf16(a[0], a[1]); w.y = cvt_pk_bf16(a[2], a[3]); w.z = cvt_pk_bf16(b[0], b[1]); w.w = cvt_pk_bf16(b[2], b[3]); return w; }
;     __device__ __forceinline__ void operator()(const f32x4 (&acc)[2][2][4][2], const Unit& u, int wr, int wc, int fr, int fq) const {
;     ...
;             for (int q = 0; q < 8; ++q) { const int ai = q >> 2, m = q & 3; const int row = row0 + ai * HALF + m * 16; const float rs = rsv[q];
;                 if (q + 1 < 8) { const size_t o = (size_t)(row0 + ((q + 1) >> 2) * HALF + ((q + 1) & 3) * 16) * 32 + fq * 8; cn[0] = *(const f32x4*)(cs + o); cn[1] = *(const f32x4*)(cs + o + 4); cn[2] = *(const f32x4*)(sn + o); cn[3] = *(const f32x4*)(sn + o + 4); }
;                 const f32x4 a0 = acc[ai][0][m][0] * rs, a1 = acc[ai][0][m][1] * rs, b0 = acc[ai][1][m][0] * rs, b1 = acc[ai][1][m][1] * rs;
;                 const f32x4 c0 = cc[0], c1 = cc[1], s0 = cc[2], s1 = cc[3];
;                 f32x4 p0 = a0 * c0 - b0 * s0, p1 = a1 * c1 - b1 * s1, r0 = b0 * c0 + a0 * s0, r1 = b1 * c1 + a1 * s1;
;                 if (t < 7) { bf16_t* d = Q + (size_t)row * 512 + ((t - 5) * 4 + wc) * 64 + fq * 8; *(u32x4*)d = pack8(p0 * qscale, p1 * qscale); *(u32x4*)(d + 32) = pack8(r0 * qscale, r1 * qscale); }
;                 else if (t < 9) { bf16_t* d = K + (size_t)row * 512 + ((t - 7) * 4 + wc) * 64 + fq * 8; *(u32x4*)d = pack8(p0, p1); *(u32x4*)(d + 32) = pack8(r0, r1); }
;                 else if (t == 11) { bf16_t* d = QI + (size_t)row * 256 + wc * 64 + fq * 8; *(u32x4*)d = pack8(p0, p1); *(u32x4*)(d + 32) = pack8(r0, r1); }
.LBB0_722:
	s_and_b64 vcc, exec, s[4:5]
	s_cbranch_vccz .LBB0_724
	v_and_b32_e32 v144, -32, v192
	v_lshlrev_b32_e32 v144, 9, v144
	v_and_b32_e32 v145, 31, v192
	v_lshl_add_u32 v144, v145, 4, v144
	v_mov_b32_e32 v145, 0
	v_lshl_add_u64 v[156:157], v[230:231], 0, v[144:145]
	v_cvt_pk_bf16_f32 v144, v170, v171
	v_cvt_pk_bf16_f32 v145, v168, v169
	v_cvt_pk_bf16_f32 v146, v238, v239
	v_cvt_pk_bf16_f32 v147, v236, v237
	global_store_dwordx4 v[156:157], v[144:147], off
	s_nop 1
	v_cvt_pk_bf16_f32 v144, v148, v149
	v_cvt_pk_bf16_f32 v145, v150, v151
	v_cvt_pk_bf16_f32 v146, v136, v137
	v_cvt_pk_bf16_f32 v147, v138, v139
	global_store_dwordx4 v[156:157], v[144:147], off offset:2048

; __device__ __forceinline__ u32x4 pack8(const f32x4 a, const f32x4 b) { u32x4 w; w.x = cvt_pk_bf16(a[0], a[1]); w.y = cvt_pk_bf16(a[2], a[3]); w.z = cvt_pk_bf16(b[0], b[1]); w.w = cvt_pk_bf16(b[2], b[3]); return w; }
;     __device__ __forceinline__ void operator()(const f32x4 (&acc)[2][2][4][2], const Unit& u, int wr, int wc, int fr, int fq) const {
;     ...
;             for (int q = 0; q < 8; ++q) { const int ai = q >> 2, m = q & 3; const int row = row0 + ai * HALF + m * 16; const float rs = rsv[q];
;                 if (q + 1 < 8) { const size_t o = (size_t)(row0 + ((q + 1) >> 2) * HALF + ((q + 1) & 3) * 16) * 32 + fq * 8; cn[0] = *(const f32x4*)(cs + o); cn[1] = *(const f32x4*)(cs + o + 4); cn[2] = *(const f32x4*)(sn + o); cn[3] = *(const f32x4*)(sn + o + 4); }
;                 const f32x4 a0 = acc[ai][0][m][0] * rs, a1 = acc[ai][0][m][1] * rs, b0 = acc[ai][1][m][0] * rs, b1 = acc[ai][1][m][1] * rs;
;                 const f32x4 c0 = cc[0], c1 = cc[1], s0 = cc[2], s1 = cc[3];
;                 f32x4 p0 = a0 * c0 - b0 * s0, p1 = a1 * c1 - b1 * s1, r0 = b0 * c0 + a0 * s0, r1 = b1 * c1 + a1 * s1;
;                 if (t < 7) { bf16_t* d = Q + (size_t)row * 512 + ((t - 5) * 4 + wc) * 64 + fq * 8; *(u32x4*)d = pack8(p0 * qscale, p1 * qscale); *(u32x4*)(d + 32) = pack8(r0 * qscale, r1 * qscale); }
;                 else if (t < 9) { bf16_t* d = K + (size_t)row * 512 + ((t - 7) * 4 + wc) * 64 + fq * 8; *(u32x4*)d = pack8(p0, p1); *(u32x4*)(d + 32) = pack8(r0, r1); }
;                 else if (t == 11) { bf16_t* d = QI + (size_t)row * 256 + wc * 64 + fq * 8; *(u32x4*)d = pack8(p0, p1); *(u32x4*)(d + 32) = pack8(r0, r1); }
.LBB0_737:
	s_and_b64 vcc, exec, s[4:5]
	s_cbranch_vccz .LBB0_739
	v_and_b32_e32 v140, -32, v188
	v_lshlrev_b32_e32 v140, 9, v140
	v_and_b32_e32 v141, 31, v188
	v_lshl_add_u32 v140, v141, 4, v140
	v_mov_b32_e32 v141, 0
	v_lshl_add_u64 v[160:161], v[230:231], 0, v[140:141]
	v_cvt_pk_bf16_f32 v140, v170, v171
	v_cvt_pk_bf16_f32 v141, v168, v169
	v_cvt_pk_bf16_f32 v142, v238, v239
	v_cvt_pk_bf16_f32 v143, v236, v237
	global_store_dwordx4 v[160:161], v[140:143], off
	s_nop 1
	v_cvt_pk_bf16_f32 v140, v152, v153
	v_cvt_pk_bf16_f32 v141, v154, v155
	v_cvt_pk_bf16_f32 v142, v132, v133
	v_cvt_pk_bf16_f32 v143, v134, v135
	global_store_dwordx4 v[160:161], v[140:143], off offset:2048

; __device__ __forceinline__ u32x4 pack8(const f32x4 a, const f32x4 b) { u32x4 w; w.x = cvt_pk_bf16(a[0], a[1]); w.y = cvt_pk_bf16(a[2], a[3]); w.z = cvt_pk_bf16(b[0], b[1]); w.w = cvt_pk_bf16(b[2], b[3]); return w; }
;     __device__ __forceinline__ void operator()(const f32x4 (&acc)[2][2][4][2], const Unit& u, int wr, int wc, int fr, int fq) const {
;     ...
;             for (int q = 0; q < 8; ++q) { const int ai = q >> 2, m = q & 3; const int row = row0 + ai * HALF + m * 16; const float rs = rsv[q];
;                 if (q + 1 < 8) { const size_t o = (size_t)(row0 + ((q + 1) >> 2) * HALF + ((q + 1) & 3) * 16) * 32 + fq * 8; cn[0] = *(const f32x4*)(cs + o); cn[1] = *(const f32x4*)(cs + o + 4); cn[2] = *(const f32x4*)(sn + o); cn[3] = *(const f32x4*)(sn + o + 4); }
;                 const f32x4 a0 = acc[ai][0][m][0] * rs, a1 = acc[ai][0][m][1] * rs, b0 = acc[ai][1][m][0] * rs, b1 = acc[ai][1][m][1] * rs;
;                 const f32x4 c0 = cc[0], c1 = cc[1], s0 = cc[2], s1 = cc[3];
;                 f32x4 p0 = a0 * c0 - b0 * s0, p1 = a1 * c1 - b1 * s1, r0 = b0 * c0 + a0 * s0, r1 = b1 * c1 + a1 * s1;
;                 if (t < 7) { bf16_t* d = Q + (size_t)row * 512 + ((t - 5) * 4 + wc) * 64 + fq * 8; *(u32x4*)d = pack8(p0 * qscale, p1 * qscale); *(u32x4*)(d + 32) = pack8(r0 * qscale, r1 * qscale); }
;                 else if (t < 9) { bf16_t* d = K + (size_t)row * 512 + ((t - 7) * 4 + wc) * 64 + fq * 8; *(u32x4*)d = pack8(p0, p1); *(u32x4*)(d + 32) = pack8(r0, r1); }
;                 else if (t == 11) { bf16_t* d = QI + (size_t)row * 256 + wc * 64 + fq * 8; *(u32x4*)d = pack8(p0, p1); *(u32x4*)(d + 32) = pack8(r0, r1); }
.LBB0_752:
	s_and_b64 vcc, exec, s[4:5]
	s_cbranch_vccz .LBB0_754
	v_and_b32_e32 v144, -32, v184
	v_lshlrev_b32_e32 v144, 9, v144
	v_and_b32_e32 v145, 31, v184
	v_lshl_add_u32 v144, v145, 4, v144
	v_mov_b32_e32 v145, 0
	v_lshl_add_u64 v[156:157], v[230:231], 0, v[144:145]
	v_cvt_pk_bf16_f32 v144, v170, v171
	v_cvt_pk_bf16_f32 v145, v168, v169
	v_cvt_pk_bf16_f32 v146, v238, v239
	v_cvt_pk_bf16_f32 v147, v236, v237
	global_store_dwordx4 v[156:157], v[144:147], off
	s_nop 1
	v_cvt_pk_bf16_f32 v144, v148, v149
	v_cvt_pk_bf16_f32 v145, v150, v151
	v_cvt_pk_bf16_f32 v146, v136, v137
	v_cvt_pk_bf16_f32 v147, v138, v139
	global_store_dwordx4 v[156:157], v[144:147], off offset:2048

; __device__ __forceinline__ u32x4 pack8(const f32x4 a, const f32x4 b) { u32x4 w; w.x = cvt_pk_bf16(a[0], a[1]); w.y = cvt_pk_bf16(a[2], a[3]); w.z = cvt_pk_bf16(b[0], b[1]); w.w = cvt_pk_bf16(b[2], b[3]); return w; }
;     __device__ __forceinline__ void operator()(const f32x4 (&acc)[2][2][4][2], const Unit& u, int wr, int wc, int fr, int fq) const {
;     ...
;             for (int q = 0; q < 8; ++q) { const int ai = q >> 2, m = q & 3; const int row = row0 + ai * HALF + m * 16; const float rs = rsv[q];
;                 if (q + 1 < 8) { const size_t o = (size_t)(row0 + ((q + 1) >> 2) * HALF + ((q + 1) & 3) * 16) * 32 + fq * 8; cn[0] = *(const f32x4*)(cs + o); cn[1] = *(const f32x4*)(cs + o + 4); cn[2] = *(const f32x4*)(sn + o); cn[3] = *(const f32x4*)(sn + o + 4); }
;                 const f32x4 a0 = acc[ai][0][m][0] * rs, a1 = acc[ai][0][m][1] * rs, b0 = acc[ai][1][m][0] * rs, b1 = acc[ai][1][m][1] * rs;
;                 const f32x4 c0 = cc[0], c1 = cc[1], s0 = cc[2], s1 = cc[3];
;                 f32x4 p0 = a0 * c0 - b0 * s0, p1 = a1 * c1 - b1 * s1, r0 = b0 * c0 + a0 * s0, r1 = b1 * c1 + a1 * s1;
;                 if (t < 7) { bf16_t* d = Q + (size_t)row * 512 + ((t - 5) * 4 + wc) * 64 + fq * 8; *(u32x4*)d = pack8(p0 * qscale, p1 * qscale); *(u32x4*)(d + 32) = pack8(r0 * qscale, r1 * qscale); }
;                 else if (t < 9) { bf16_t* d = K + (size_t)row * 512 + ((t - 7) * 4 + wc) * 64 + fq * 8; *(u32x4*)d = pack8(p0, p1); *(u32x4*)(d + 32) = pack8(r0, r1); }
;                 else if (t == 11) { bf16_t* d = QI + (size_t)row * 256 + wc * 64 + fq * 8; *(u32x4*)d = pack8(p0, p1); *(u32x4*)(d + 32) = pack8(r0, r1); }
.LBB0_767:
	s_and_b64 vcc, exec, s[4:5]
	s_cbranch_vccz .LBB0_769
	v_and_b32_e32 v136, -32, v182
	v_lshlrev_b32_e32 v136, 9, v136
	v_and_b32_e32 v137, 31, v182
	v_lshl_add_u32 v136, v137, 4, v136
	v_mov_b32_e32 v137, 0
	v_lshl_add_u64 v[140:141], v[230:231], 0, v[136:137]
	v_cvt_pk_bf16_f32 v136, v150, v151
	v_cvt_pk_bf16_f32 v137, v148, v149
	v_cvt_pk_bf16_f32 v138, v158, v159
	v_cvt_pk_bf16_f32 v139, v156, v157
	global_store_dwordx4 v[140:141], v[136:139], off
	s_nop 1
	v_cvt_pk_bf16_f32 v136, v146, v147
	v_cvt_pk_bf16_f32 v137, v144, v145
	v_cvt_pk_bf16_f32 v138, v132, v133
	v_cvt_pk_bf16_f32 v139, v134, v135
	global_store_dwordx4 v[140:141], v[136:139], off offset:2048

; #define GAS __attribute__((address_space(1)))
; __device__ __forceinline__ void idx_unit(Frame& F, const bf16* QI, const bf16* KI, const float* WI, unsigned* MASK, int b, int j) {
;     ...
;     const size_t qrow = (size_t)b * SEQ + 32 * j + r32;
;     bf16x8 bq[4][4];
; #pragma unroll
;     for (int h = 0; h < 4; ++h)
; #pragma unroll
;         for (int kk = 0; kk < 4; ++kk) bq[h][kk] = *(const GAS bf16x8*)(QI + qrow * 256 + h * 64 + kk * 16 + hi * 8);
;     f32x4 wv = *(const GAS f32x4*)(WI + qrow * 4); wv = wv * IDX_SCALE;
.LBB0_972:
	s_bfe_u32 s76, s17, 0x20006
	s_lshl_b32 s4, s76, 13
	s_lshl_b32 s5, s84, 5
	s_add_i32 s4, s4, s5
	v_or_b32_e32 v4, s4, v194
	v_mov_b32_e32 v5, v195
	s_lshl_b32 s8, s4, 9
	v_sub_u32_e32 v8, v226, v228
	v_lshl_add_u32 v6, v8, 4, s8
	v_mov_b32_e32 v7, 0
	s_mov_b64 s[40:41], 0x1000
	v_lshl_add_u64 v[6:7], v[208:209], 0, v[6:7]
	v_lshl_add_u64 v[8:9], v[6:7], 0, s[40:41]
	v_lshl_add_u64 v[10:11], v[8:9], 0, s[40:41]
	v_lshl_add_u64 v[12:13], v[10:11], 0, s[40:41]
	global_load_dwordx4 v[82:85], v[6:7], off
	global_load_dwordx4 v[86:89], v[6:7], off offset:1024
	global_load_dwordx4 v[90:93], v[6:7], off offset:2048
	global_load_dwordx4 v[94:97], v[6:7], off offset:3072
	global_load_dwordx4 v[98:101], v[8:9], off
	global_load_dwordx4 v[102:105], v[8:9], off offset:1024
	global_load_dwordx4 v[106:109], v[8:9], off offset:2048
	global_load_dwordx4 v[110:113], v[8:9], off offset:3072
	global_load_dwordx4 v[114:117], v[10:11], off
	global_load_dwordx4 v[118:121], v[10:11], off offset:1024
	global_load_dwordx4 v[122:125], v[10:11], off offset:2048
	global_load_dwordx4 v[126:129], v[10:11], off offset:3072
	global_load_dwordx4 v[130:133], v[12:13], off
	global_load_dwordx4 v[134:137], v[12:13], off offset:1024
	global_load_dwordx4 v[138:141], v[12:13], off offset:2048
	global_load_dwordx4 v[142:145], v[12:13], off offset:3072
	v_lshl_add_u64 v[4:5], v[4:5], 4, s[88:89]
	global_load_dwordx4 v[4:7], v[4:5], off
	s_cmp_gt_u32 s84, 7
	s_mov_b32 s4, 0x3d800000
	s_cselect_b64 s[94:95], -1, 0
	s_and_b64 vcc, exec, s[94:95]
	s_waitcnt vmcnt(0)
	v_pk_mul_f32 v[214:215], v[6:7], s[4:5] op_sel_hi:[1,0]
	v_pk_mul_f32 v[216:217], v[4:5], s[4:5] op_sel_hi:[1,0]
	s_mov_b64 s[4:5], -1
	s_cbranch_vccnz .LBB0_974
	s_mov_b64 s[4:5], 0
	v_mov_b32_e32 v2, v215
